# v44 + accumulator zeroing with 64 v_mov_b64 instead of 128 v_mov_b32 at every GEMM tile head
# speedup vs baseline: 1.0109x; 1.0109x over previous
; template <class Epi, class Sched, bool ALIGN_EPI = true, bool F8 = false>
; __device__ __forceinline__ void gemm_phase(PG8_LAS unsigned char* lds, const Sched& S, const Epi& E) {
;     ...
; #pragma unroll
;         for (int a = 0; a < 2; ++a)
; #pragma unroll
;             for (int b = 0; b < 2; ++b)
; #pragma unroll
;                 for (int m = 0; m < 4; ++m)
; #pragma unroll
;                     for (int n = 0; n < 2; ++n) acc[a][b][m][n] = (f32x4){0.f, 0.f, 0.f, 0.f};
;         }
.LBB0_371:
	s_add_u32 s5, s28, 0x10000
	s_addc_u32 s19, s29, 0
	s_add_u32 s26, s26, 0x8000
	v_mov_b64_e32 v[34:35], 0
	s_addc_u32 s27, s27, 0
	s_mov_b32 s21, -2
	v_mov_b64_e32 v[36:37], 0
	v_mov_b64_e32 v[38:39], 0
	v_mov_b64_e32 v[40:41], 0
	v_mov_b64_e32 v[50:51], 0
	v_mov_b64_e32 v[52:53], 0
	v_mov_b64_e32 v[54:55], 0
	v_mov_b64_e32 v[56:57], 0
	v_mov_b64_e32 v[66:67], 0
	v_mov_b64_e32 v[68:69], 0
	v_mov_b64_e32 v[70:71], 0
	v_mov_b64_e32 v[72:73], 0
	v_mov_b64_e32 v[82:83], 0
	v_mov_b64_e32 v[84:85], 0
	v_mov_b64_e32 v[86:87], 0
	v_mov_b64_e32 v[88:89], 0
	v_mov_b64_e32 v[42:43], 0
	v_mov_b64_e32 v[44:45], 0
	v_mov_b64_e32 v[46:47], 0
	v_mov_b64_e32 v[48:49], 0
	v_mov_b64_e32 v[58:59], 0
	v_mov_b64_e32 v[60:61], 0
	v_mov_b64_e32 v[62:63], 0
	v_mov_b64_e32 v[64:65], 0
	v_mov_b64_e32 v[74:75], 0
	v_mov_b64_e32 v[76:77], 0
	v_mov_b64_e32 v[78:79], 0
	v_mov_b64_e32 v[80:81], 0
	v_mov_b64_e32 v[90:91], 0
	v_mov_b64_e32 v[92:93], 0
	v_mov_b64_e32 v[94:95], 0
	v_mov_b64_e32 v[96:97], 0
	v_mov_b64_e32 v[98:99], 0
	v_mov_b64_e32 v[100:101], 0
	v_mov_b64_e32 v[102:103], 0
	v_mov_b64_e32 v[104:105], 0
	v_mov_b64_e32 v[114:115], 0
	v_mov_b64_e32 v[116:117], 0
	v_mov_b64_e32 v[118:119], 0
	v_mov_b64_e32 v[120:121], 0
	v_mov_b64_e32 v[130:131], 0
	v_mov_b64_e32 v[132:133], 0
	v_mov_b64_e32 v[134:135], 0
	v_mov_b64_e32 v[136:137], 0
	v_mov_b64_e32 v[146:147], 0
	v_mov_b64_e32 v[148:149], 0
	v_mov_b64_e32 v[150:151], 0
	v_mov_b64_e32 v[152:153], 0
	v_mov_b64_e32 v[106:107], 0
	v_mov_b64_e32 v[108:109], 0
	v_mov_b64_e32 v[110:111], 0
	v_mov_b64_e32 v[112:113], 0
	v_mov_b64_e32 v[122:123], 0
	v_mov_b64_e32 v[124:125], 0
	v_mov_b64_e32 v[126:127], 0
	v_mov_b64_e32 v[128:129], 0
	v_mov_b64_e32 v[138:139], 0
	v_mov_b64_e32 v[140:141], 0
	v_mov_b64_e32 v[142:143], 0
	v_mov_b64_e32 v[144:145], 0
	v_mov_b64_e32 v[154:155], 0
	v_mov_b64_e32 v[156:157], 0
	v_mov_b64_e32 v[158:159], 0
	v_mov_b64_e32 v[160:161], 0
	s_bitcmp1_b32 s3, 2
	s_cbranch_scc1 .Lh1e_9967

; template <class Epi, class Sched, bool ALIGN_EPI = true, bool F8 = false>
; __device__ __forceinline__ void gemm_phase(PG8_LAS unsigned char* lds, const Sched& S, const Epi& E) {
;     ...
; #pragma unroll
;         for (int a = 0; a < 2; ++a)
; #pragma unroll
;             for (int b = 0; b < 2; ++b)
; #pragma unroll
;                 for (int m = 0; m < 4; ++m)
; #pragma unroll
;                     for (int n = 0; n < 2; ++n) acc[a][b][m][n] = (f32x4){0.f, 0.f, 0.f, 0.f};
;         }
.LBB0_427:
	s_add_u32 s17, s26, 0x10000
	s_addc_u32 s19, s27, 0
	s_add_u32 s24, s24, 0x8000
	v_mov_b64_e32 v[34:35], 0
	s_addc_u32 s25, s25, 0
	s_mov_b32 s74, -2
	v_mov_b64_e32 v[36:37], 0
	v_mov_b64_e32 v[38:39], 0
	v_mov_b64_e32 v[40:41], 0
	v_mov_b64_e32 v[50:51], 0
	v_mov_b64_e32 v[52:53], 0
	v_mov_b64_e32 v[54:55], 0
	v_mov_b64_e32 v[56:57], 0
	v_mov_b64_e32 v[66:67], 0
	v_mov_b64_e32 v[68:69], 0
	v_mov_b64_e32 v[70:71], 0
	v_mov_b64_e32 v[72:73], 0
	v_mov_b64_e32 v[82:83], 0
	v_mov_b64_e32 v[84:85], 0
	v_mov_b64_e32 v[86:87], 0
	v_mov_b64_e32 v[88:89], 0
	v_mov_b64_e32 v[42:43], 0
	v_mov_b64_e32 v[44:45], 0
	v_mov_b64_e32 v[46:47], 0
	v_mov_b64_e32 v[48:49], 0
	v_mov_b64_e32 v[58:59], 0
	v_mov_b64_e32 v[60:61], 0
	v_mov_b64_e32 v[62:63], 0
	v_mov_b64_e32 v[64:65], 0
	v_mov_b64_e32 v[74:75], 0
	v_mov_b64_e32 v[76:77], 0
	v_mov_b64_e32 v[78:79], 0
	v_mov_b64_e32 v[80:81], 0
	v_mov_b64_e32 v[90:91], 0
	v_mov_b64_e32 v[92:93], 0
	v_mov_b64_e32 v[94:95], 0
	v_mov_b64_e32 v[96:97], 0
	v_mov_b64_e32 v[98:99], 0
	v_mov_b64_e32 v[100:101], 0
	v_mov_b64_e32 v[102:103], 0
	v_mov_b64_e32 v[104:105], 0
	v_mov_b64_e32 v[114:115], 0
	v_mov_b64_e32 v[116:117], 0
	v_mov_b64_e32 v[118:119], 0
	v_mov_b64_e32 v[120:121], 0
	v_mov_b64_e32 v[130:131], 0
	v_mov_b64_e32 v[132:133], 0
	v_mov_b64_e32 v[134:135], 0
	v_mov_b64_e32 v[136:137], 0
	v_mov_b64_e32 v[146:147], 0
	v_mov_b64_e32 v[148:149], 0
	v_mov_b64_e32 v[150:151], 0
	v_mov_b64_e32 v[152:153], 0
	v_mov_b64_e32 v[106:107], 0
	v_mov_b64_e32 v[108:109], 0
	v_mov_b64_e32 v[110:111], 0
	v_mov_b64_e32 v[112:113], 0
	v_mov_b64_e32 v[122:123], 0
	v_mov_b64_e32 v[124:125], 0
	v_mov_b64_e32 v[126:127], 0
	v_mov_b64_e32 v[128:129], 0
	v_mov_b64_e32 v[138:139], 0
	v_mov_b64_e32 v[140:141], 0
	v_mov_b64_e32 v[142:143], 0
	v_mov_b64_e32 v[144:145], 0
	v_mov_b64_e32 v[154:155], 0
	v_mov_b64_e32 v[156:157], 0
	v_mov_b64_e32 v[158:159], 0
	v_mov_b64_e32 v[160:161], 0
	s_bitcmp1_b32 s3, 2
	s_cbranch_scc1 .Lh1e_11141

; template <class Epi, class Sched, bool ALIGN_EPI = true, bool F8 = false>
; __device__ __forceinline__ void gemm_phase(PG8_LAS unsigned char* lds, const Sched& S, const Epi& E) {
;     ...
; #pragma unroll
;         for (int a = 0; a < 2; ++a)
; #pragma unroll
;             for (int b = 0; b < 2; ++b)
; #pragma unroll
;                 for (int m = 0; m < 4; ++m)
; #pragma unroll
;                     for (int n = 0; n < 2; ++n) acc[a][b][m][n] = (f32x4){0.f, 0.f, 0.f, 0.f};
;         }
.LBB0_490:
	s_add_u32 s15, s24, 0x100
	v_mov_b64_e32 v[2:3], 0
	s_addc_u32 s65, s25, 0
	s_mov_b32 s66, -2
	v_mov_b64_e32 v[4:5], 0
	v_mov_b64_e32 v[6:7], 0
	v_mov_b64_e32 v[8:9], 0
	v_mov_b64_e32 v[10:11], 0
	v_mov_b64_e32 v[12:13], 0
	v_mov_b64_e32 v[14:15], 0
	v_mov_b64_e32 v[16:17], 0
	v_mov_b64_e32 v[18:19], 0
	v_mov_b64_e32 v[20:21], 0
	v_mov_b64_e32 v[22:23], 0
	v_mov_b64_e32 v[24:25], 0
	v_mov_b64_e32 v[30:31], 0
	v_mov_b64_e32 v[32:33], 0
	v_mov_b64_e32 v[38:39], 0
	v_mov_b64_e32 v[40:41], 0
	v_mov_b64_e32 v[26:27], 0
	v_mov_b64_e32 v[28:29], 0
	v_mov_b64_e32 v[34:35], 0
	v_mov_b64_e32 v[36:37], 0
	v_mov_b64_e32 v[42:43], 0
	v_mov_b64_e32 v[44:45], 0
	v_mov_b64_e32 v[46:47], 0
	v_mov_b64_e32 v[48:49], 0
	v_mov_b64_e32 v[50:51], 0
	v_mov_b64_e32 v[52:53], 0
	v_mov_b64_e32 v[54:55], 0
	v_mov_b64_e32 v[56:57], 0
	v_mov_b64_e32 v[58:59], 0
	v_mov_b64_e32 v[60:61], 0
	v_mov_b64_e32 v[62:63], 0
	v_mov_b64_e32 v[64:65], 0
	v_mov_b64_e32 v[66:67], 0
	v_mov_b64_e32 v[68:69], 0
	v_mov_b64_e32 v[70:71], 0
	v_mov_b64_e32 v[72:73], 0
	v_mov_b64_e32 v[74:75], 0
	v_mov_b64_e32 v[76:77], 0
	v_mov_b64_e32 v[78:79], 0
	v_mov_b64_e32 v[80:81], 0
	v_mov_b64_e32 v[82:83], 0
	v_mov_b64_e32 v[84:85], 0
	v_mov_b64_e32 v[86:87], 0
	v_mov_b64_e32 v[88:89], 0
	v_mov_b64_e32 v[94:95], 0
	v_mov_b64_e32 v[96:97], 0
	v_mov_b64_e32 v[102:103], 0
	v_mov_b64_e32 v[104:105], 0
	v_mov_b64_e32 v[90:91], 0
	v_mov_b64_e32 v[92:93], 0
	v_mov_b64_e32 v[98:99], 0
	v_mov_b64_e32 v[100:101], 0
	v_mov_b64_e32 v[106:107], 0
	v_mov_b64_e32 v[108:109], 0
	v_mov_b64_e32 v[110:111], 0
	v_mov_b64_e32 v[112:113], 0
	v_mov_b64_e32 v[114:115], 0
	v_mov_b64_e32 v[116:117], 0
	v_mov_b64_e32 v[118:119], 0
	v_mov_b64_e32 v[120:121], 0
	v_mov_b64_e32 v[122:123], 0
	v_mov_b64_e32 v[124:125], 0
	v_mov_b64_e32 v[126:127], 0
	v_mov_b64_e32 v[128:129], 0

; template <class Epi, class Sched, bool ALIGN_EPI = true, bool F8 = false>
; __device__ __forceinline__ void gemm_phase(PG8_LAS unsigned char* lds, const Sched& S, const Epi& E) {
;     ...
; #pragma unroll
;         for (int a = 0; a < 2; ++a)
; #pragma unroll
;             for (int b = 0; b < 2; ++b)
; #pragma unroll
;                 for (int m = 0; m < 4; ++m)
; #pragma unroll
;                     for (int n = 0; n < 2; ++n) acc[a][b][m][n] = (f32x4){0.f, 0.f, 0.f, 0.f};
;         }
.LBB0_513:
	v_mov_b64_e32 v[2:3], 0
	s_mov_b32 s15, 0
	s_mov_b64 s[30:31], -1
	s_mov_b64 s[40:41], 0
	v_mov_b64_e32 v[4:5], 0
	v_mov_b64_e32 v[6:7], 0
	v_mov_b64_e32 v[8:9], 0
	v_mov_b64_e32 v[10:11], 0
	v_mov_b64_e32 v[12:13], 0
	v_mov_b64_e32 v[14:15], 0
	v_mov_b64_e32 v[16:17], 0
	v_mov_b64_e32 v[26:27], 0
	v_mov_b64_e32 v[28:29], 0
	v_mov_b64_e32 v[30:31], 0
	v_mov_b64_e32 v[32:33], 0
	v_mov_b64_e32 v[42:43], 0
	v_mov_b64_e32 v[44:45], 0
	v_mov_b64_e32 v[46:47], 0
	v_mov_b64_e32 v[48:49], 0
	v_mov_b64_e32 v[18:19], 0
	v_mov_b64_e32 v[20:21], 0
	v_mov_b64_e32 v[22:23], 0
	v_mov_b64_e32 v[24:25], 0
	v_mov_b64_e32 v[34:35], 0
	v_mov_b64_e32 v[36:37], 0
	v_mov_b64_e32 v[38:39], 0
	v_mov_b64_e32 v[40:41], 0
	v_mov_b64_e32 v[50:51], 0
	v_mov_b64_e32 v[52:53], 0
	v_mov_b64_e32 v[54:55], 0
	v_mov_b64_e32 v[56:57], 0
	v_mov_b64_e32 v[58:59], 0
	v_mov_b64_e32 v[60:61], 0
	v_mov_b64_e32 v[62:63], 0
	v_mov_b64_e32 v[64:65], 0
	v_mov_b64_e32 v[66:67], 0
	v_mov_b64_e32 v[68:69], 0
	v_mov_b64_e32 v[70:71], 0
	v_mov_b64_e32 v[72:73], 0
	v_mov_b64_e32 v[74:75], 0
	v_mov_b64_e32 v[76:77], 0
	v_mov_b64_e32 v[78:79], 0
	v_mov_b64_e32 v[80:81], 0
	v_mov_b64_e32 v[90:91], 0
	v_mov_b64_e32 v[92:93], 0
	v_mov_b64_e32 v[94:95], 0
	v_mov_b64_e32 v[96:97], 0
	v_mov_b64_e32 v[106:107], 0
	v_mov_b64_e32 v[108:109], 0
	v_mov_b64_e32 v[110:111], 0
	v_mov_b64_e32 v[112:113], 0
	v_mov_b64_e32 v[82:83], 0
	v_mov_b64_e32 v[84:85], 0
	v_mov_b64_e32 v[86:87], 0
	v_mov_b64_e32 v[88:89], 0
	v_mov_b64_e32 v[98:99], 0
	v_mov_b64_e32 v[100:101], 0
	v_mov_b64_e32 v[102:103], 0
	v_mov_b64_e32 v[104:105], 0
	v_mov_b64_e32 v[114:115], 0
	v_mov_b64_e32 v[116:117], 0
	v_mov_b64_e32 v[118:119], 0
	v_mov_b64_e32 v[120:121], 0
	v_mov_b64_e32 v[122:123], 0
	v_mov_b64_e32 v[124:125], 0
	v_mov_b64_e32 v[126:127], 0
	v_mov_b64_e32 v[128:129], 0

; template <class Epi, class Sched, bool ALIGN_EPI = true, bool F8 = false>
; __device__ __forceinline__ void gemm_phase(PG8_LAS unsigned char* lds, const Sched& S, const Epi& E) {
;     ...
; #pragma unroll
;         for (int a = 0; a < 2; ++a)
; #pragma unroll
;             for (int b = 0; b < 2; ++b)
; #pragma unroll
;                 for (int m = 0; m < 4; ++m)
; #pragma unroll
;                     for (int n = 0; n < 2; ++n) acc[a][b][m][n] = (f32x4){0.f, 0.f, 0.f, 0.f};
;         }
.LBB0_675:
	s_add_u32 s63, s22, 0x100
	v_mov_b64_e32 v[2:3], 0
	s_addc_u32 s64, s23, 0
	s_mov_b32 s65, -2
	v_mov_b64_e32 v[4:5], 0
	v_mov_b64_e32 v[6:7], 0
	v_mov_b64_e32 v[8:9], 0
	v_mov_b64_e32 v[18:19], 0
	v_mov_b64_e32 v[20:21], 0
	v_mov_b64_e32 v[22:23], 0
	v_mov_b64_e32 v[24:25], 0
	v_mov_b64_e32 v[34:35], 0
	v_mov_b64_e32 v[36:37], 0
	v_mov_b64_e32 v[38:39], 0
	v_mov_b64_e32 v[40:41], 0
	v_mov_b64_e32 v[50:51], 0
	v_mov_b64_e32 v[52:53], 0
	v_mov_b64_e32 v[54:55], 0
	v_mov_b64_e32 v[56:57], 0
	v_mov_b64_e32 v[10:11], 0
	v_mov_b64_e32 v[12:13], 0
	v_mov_b64_e32 v[14:15], 0
	v_mov_b64_e32 v[16:17], 0
	v_mov_b64_e32 v[26:27], 0
	v_mov_b64_e32 v[28:29], 0
	v_mov_b64_e32 v[30:31], 0
	v_mov_b64_e32 v[32:33], 0
	v_mov_b64_e32 v[42:43], 0
	v_mov_b64_e32 v[44:45], 0
	v_mov_b64_e32 v[46:47], 0
	v_mov_b64_e32 v[48:49], 0
	v_mov_b64_e32 v[58:59], 0
	v_mov_b64_e32 v[60:61], 0
	v_mov_b64_e32 v[62:63], 0
	v_mov_b64_e32 v[64:65], 0
	v_mov_b64_e32 v[66:67], 0
	v_mov_b64_e32 v[68:69], 0
	v_mov_b64_e32 v[70:71], 0
	v_mov_b64_e32 v[72:73], 0
	v_mov_b64_e32 v[82:83], 0
	v_mov_b64_e32 v[84:85], 0
	v_mov_b64_e32 v[86:87], 0
	v_mov_b64_e32 v[88:89], 0
	v_mov_b64_e32 v[98:99], 0
	v_mov_b64_e32 v[100:101], 0
	v_mov_b64_e32 v[102:103], 0
	v_mov_b64_e32 v[104:105], 0
	v_mov_b64_e32 v[114:115], 0
	v_mov_b64_e32 v[116:117], 0
	v_mov_b64_e32 v[118:119], 0
	v_mov_b64_e32 v[120:121], 0
	v_mov_b64_e32 v[74:75], 0
	v_mov_b64_e32 v[76:77], 0
	v_mov_b64_e32 v[78:79], 0
	v_mov_b64_e32 v[80:81], 0
	v_mov_b64_e32 v[90:91], 0
	v_mov_b64_e32 v[92:93], 0
	v_mov_b64_e32 v[94:95], 0
	v_mov_b64_e32 v[96:97], 0
	v_mov_b64_e32 v[106:107], 0
	v_mov_b64_e32 v[108:109], 0
	v_mov_b64_e32 v[110:111], 0
	v_mov_b64_e32 v[112:113], 0
	v_mov_b64_e32 v[122:123], 0
	v_mov_b64_e32 v[124:125], 0
	v_mov_b64_e32 v[126:127], 0
	v_mov_b64_e32 v[128:129], 0

; template <class Epi, class Sched, bool ALIGN_EPI = true, bool F8 = false>
; __device__ __forceinline__ void gemm_phase(PG8_LAS unsigned char* lds, const Sched& S, const Epi& E) {
;     ...
; #pragma unroll
;         for (int a = 0; a < 2; ++a)
; #pragma unroll
;             for (int b = 0; b < 2; ++b)
; #pragma unroll
;                 for (int m = 0; m < 4; ++m)
; #pragma unroll
;                     for (int n = 0; n < 2; ++n) acc[a][b][m][n] = (f32x4){0.f, 0.f, 0.f, 0.f};
;         }
.LBB0_691:
	v_mov_b64_e32 v[2:3], 0
	s_mov_b32 s19, 0
	s_mov_b64 s[22:23], -1
	s_mov_b64 s[24:25], 0
	v_mov_b64_e32 v[4:5], 0
	v_mov_b64_e32 v[6:7], 0
	v_mov_b64_e32 v[8:9], 0
	v_mov_b64_e32 v[14:15], 0
	v_mov_b64_e32 v[16:17], 0
	v_mov_b64_e32 v[22:23], 0
	v_mov_b64_e32 v[24:25], 0
	v_mov_b64_e32 v[30:31], 0
	v_mov_b64_e32 v[32:33], 0
	v_mov_b64_e32 v[38:39], 0
	v_mov_b64_e32 v[40:41], 0
	v_mov_b64_e32 v[46:47], 0
	v_mov_b64_e32 v[48:49], 0
	v_mov_b64_e32 v[54:55], 0
	v_mov_b64_e32 v[56:57], 0
	v_mov_b64_e32 v[10:11], 0
	v_mov_b64_e32 v[12:13], 0
	v_mov_b64_e32 v[18:19], 0
	v_mov_b64_e32 v[20:21], 0
	v_mov_b64_e32 v[26:27], 0
	v_mov_b64_e32 v[28:29], 0
	v_mov_b64_e32 v[34:35], 0
	v_mov_b64_e32 v[36:37], 0
	v_mov_b64_e32 v[42:43], 0
	v_mov_b64_e32 v[44:45], 0
	v_mov_b64_e32 v[50:51], 0
	v_mov_b64_e32 v[52:53], 0
	v_mov_b64_e32 v[58:59], 0
	v_mov_b64_e32 v[60:61], 0
	v_mov_b64_e32 v[62:63], 0
	v_mov_b64_e32 v[64:65], 0

; template <class Epi, class Sched, bool ALIGN_EPI = true, bool F8 = false>
; __device__ __forceinline__ void gemm_phase(PG8_LAS unsigned char* lds, const Sched& S, const Epi& E) {
;     ...
; #pragma unroll
;         for (int a = 0; a < 2; ++a)
; #pragma unroll
;             for (int b = 0; b < 2; ++b)
; #pragma unroll
;                 for (int m = 0; m < 4; ++m)
; #pragma unroll
;                     for (int n = 0; n < 2; ++n) acc[a][b][m][n] = (f32x4){0.f, 0.f, 0.f, 0.f};
;         }
.LBB0_762:
	s_add_u32 s19, s28, 0x100
	s_addc_u32 s21, s29, 0
	s_add_u32 s26, s26, 0x80
	v_mov_b64_e32 v[2:3], 0
	s_addc_u32 s27, s27, 0
	s_mov_b32 s69, -2
	v_mov_b64_e32 v[4:5], 0
	v_mov_b64_e32 v[6:7], 0
	v_mov_b64_e32 v[8:9], 0
	v_mov_b64_e32 v[18:19], 0
	v_mov_b64_e32 v[20:21], 0
	v_mov_b64_e32 v[22:23], 0
	v_mov_b64_e32 v[24:25], 0
	v_mov_b64_e32 v[34:35], 0
	v_mov_b64_e32 v[36:37], 0
	v_mov_b64_e32 v[38:39], 0
	v_mov_b64_e32 v[40:41], 0
	v_mov_b64_e32 v[50:51], 0
	v_mov_b64_e32 v[52:53], 0
	v_mov_b64_e32 v[54:55], 0
	v_mov_b64_e32 v[56:57], 0
	v_mov_b64_e32 v[10:11], 0
	v_mov_b64_e32 v[12:13], 0
	v_mov_b64_e32 v[14:15], 0
	v_mov_b64_e32 v[16:17], 0
	v_mov_b64_e32 v[26:27], 0
	v_mov_b64_e32 v[28:29], 0
	v_mov_b64_e32 v[30:31], 0
	v_mov_b64_e32 v[32:33], 0
	v_mov_b64_e32 v[42:43], 0
	v_mov_b64_e32 v[44:45], 0
	v_mov_b64_e32 v[46:47], 0
	v_mov_b64_e32 v[48:49], 0
	v_mov_b64_e32 v[58:59], 0
	v_mov_b64_e32 v[60:61], 0
	v_mov_b64_e32 v[66:67], 0
	v_mov_b64_e32 v[68:69], 0
	v_mov_b64_e32 v[82:83], 0
	v_mov_b64_e32 v[84:85], 0
	v_mov_b64_e32 v[86:87], 0
	v_mov_b64_e32 v[88:89], 0
	v_mov_b64_e32 v[98:99], 0
	v_mov_b64_e32 v[100:101], 0
	v_mov_b64_e32 v[102:103], 0
	v_mov_b64_e32 v[104:105], 0
	v_mov_b64_e32 v[114:115], 0
	v_mov_b64_e32 v[116:117], 0
	v_mov_b64_e32 v[118:119], 0
	v_mov_b64_e32 v[120:121], 0
	v_mov_b64_e32 v[130:131], 0
	v_mov_b64_e32 v[132:133], 0
	v_mov_b64_e32 v[134:135], 0
	v_mov_b64_e32 v[136:137], 0
	v_mov_b64_e32 v[90:91], 0
	v_mov_b64_e32 v[92:93], 0
	v_mov_b64_e32 v[94:95], 0
	v_mov_b64_e32 v[96:97], 0
	v_mov_b64_e32 v[106:107], 0
	v_mov_b64_e32 v[108:109], 0
	v_mov_b64_e32 v[110:111], 0
	v_mov_b64_e32 v[112:113], 0
	v_mov_b64_e32 v[122:123], 0
	v_mov_b64_e32 v[124:125], 0
	v_mov_b64_e32 v[126:127], 0
	v_mov_b64_e32 v[128:129], 0
	v_mov_b64_e32 v[142:143], 0
	v_mov_b64_e32 v[144:145], 0
	v_mov_b64_e32 v[146:147], 0
	v_mov_b64_e32 v[148:149], 0

; template <class Epi, class Sched, bool ALIGN_EPI = true, bool F8 = false>
; __device__ __forceinline__ void gemm_phase(PG8_LAS unsigned char* lds, const Sched& S, const Epi& E) {
;     ...
; #pragma unroll
;         for (int a = 0; a < 2; ++a)
; #pragma unroll
;             for (int b = 0; b < 2; ++b)
; #pragma unroll
;                 for (int m = 0; m < 4; ++m)
; #pragma unroll
;                     for (int n = 0; n < 2; ++n) acc[a][b][m][n] = (f32x4){0.f, 0.f, 0.f, 0.f};
;         }
.LBB0_910:
	s_add_u32 s19, s30, 0x10000
	s_addc_u32 s21, s31, 0
	s_add_u32 s28, s28, 0x8000
	v_mov_b64_e32 v[34:35], 0
	s_addc_u32 s29, s29, 0
	s_mov_b32 s65, -2
	v_mov_b64_e32 v[36:37], 0
	v_mov_b64_e32 v[38:39], 0
	v_mov_b64_e32 v[40:41], 0
	v_mov_b64_e32 v[46:47], 0
	v_mov_b64_e32 v[48:49], 0
	v_mov_b64_e32 v[54:55], 0
	v_mov_b64_e32 v[56:57], 0
	v_mov_b64_e32 v[62:63], 0
	v_mov_b64_e32 v[64:65], 0
	v_mov_b64_e32 v[70:71], 0
	v_mov_b64_e32 v[72:73], 0
	v_mov_b64_e32 v[78:79], 0
	v_mov_b64_e32 v[80:81], 0
	v_mov_b64_e32 v[86:87], 0
	v_mov_b64_e32 v[88:89], 0
	v_mov_b64_e32 v[42:43], 0
	v_mov_b64_e32 v[44:45], 0
	v_mov_b64_e32 v[50:51], 0
	v_mov_b64_e32 v[52:53], 0
	v_mov_b64_e32 v[58:59], 0
	v_mov_b64_e32 v[60:61], 0
	v_mov_b64_e32 v[66:67], 0
	v_mov_b64_e32 v[68:69], 0
	v_mov_b64_e32 v[74:75], 0
	v_mov_b64_e32 v[76:77], 0
	v_mov_b64_e32 v[82:83], 0
	v_mov_b64_e32 v[84:85], 0
	v_mov_b64_e32 v[90:91], 0
	v_mov_b64_e32 v[92:93], 0
	v_mov_b64_e32 v[94:95], 0
	v_mov_b64_e32 v[96:97], 0
	v_mov_b64_e32 v[98:99], 0
	v_mov_b64_e32 v[100:101], 0
	v_mov_b64_e32 v[102:103], 0
	v_mov_b64_e32 v[104:105], 0
	v_mov_b64_e32 v[110:111], 0
	v_mov_b64_e32 v[112:113], 0
	v_mov_b64_e32 v[118:119], 0
	v_mov_b64_e32 v[120:121], 0
	v_mov_b64_e32 v[126:127], 0
	v_mov_b64_e32 v[128:129], 0
	v_mov_b64_e32 v[134:135], 0
	v_mov_b64_e32 v[136:137], 0
	v_mov_b64_e32 v[138:139], 0
	v_mov_b64_e32 v[140:141], 0
	v_mov_b64_e32 v[142:143], 0
	v_mov_b64_e32 v[144:145], 0
	v_mov_b64_e32 v[106:107], 0
	v_mov_b64_e32 v[108:109], 0
	v_mov_b64_e32 v[114:115], 0
	v_mov_b64_e32 v[116:117], 0
	v_mov_b64_e32 v[122:123], 0
	v_mov_b64_e32 v[124:125], 0
	v_mov_b64_e32 v[130:131], 0
	v_mov_b64_e32 v[132:133], 0
	v_mov_b64_e32 v[146:147], 0
	v_mov_b64_e32 v[148:149], 0
	v_mov_b64_e32 v[150:151], 0
	v_mov_b64_e32 v[152:153], 0
	v_mov_b64_e32 v[154:155], 0
	v_mov_b64_e32 v[156:157], 0
	v_mov_b64_e32 v[158:159], 0
	v_mov_b64_e32 v[160:161], 0
	s_bitcmp1_b32 s3, 2
	s_cbranch_scc1 .Lh1e_26630

; template <class Epi, class Sched, bool ALIGN_EPI = true, bool F8 = false>
; __device__ __forceinline__ void gemm_phase(PG8_LAS unsigned char* lds, const Sched& S, const Epi& E) {
;     ...
; #pragma unroll
;         for (int a = 0; a < 2; ++a)
; #pragma unroll
;             for (int b = 0; b < 2; ++b)
; #pragma unroll
;                 for (int m = 0; m < 4; ++m)
; #pragma unroll
;                     for (int n = 0; n < 2; ++n) acc[a][b][m][n] = (f32x4){0.f, 0.f, 0.f, 0.f};
;         }
;         cur = nxt; cA = nA; cB = nB; ++ui;
; #pragma unroll
;         for (int h = 0; h < 2; ++h)
; #pragma unroll
;             for (int i = 0; i < 2; ++i) voffA[h][i] = voffAn[h][i];
.LBB0_1051:
	v_mov_b64_e32 v[34:35], 0
	v_mov_b32_e32 v174, v219
	v_mov_b32_e32 v176, v220
	v_mov_b32_e32 v172, v217
	v_mov_b32_e32 v216, v218
	s_mov_b32 s50, s66
	s_mov_b32 s0, s20
	s_mov_b32 s49, s64
	s_mov_b32 s51, s65
	s_mov_b64 s[8:9], s[24:25]
	s_mov_b32 s13, s67
	v_mov_b64_e32 v[36:37], 0
	v_mov_b64_e32 v[38:39], 0
	v_mov_b64_e32 v[40:41], 0
	v_mov_b64_e32 v[42:43], 0
	v_mov_b64_e32 v[44:45], 0
	v_mov_b64_e32 v[46:47], 0
	v_mov_b64_e32 v[48:49], 0
	v_mov_b64_e32 v[50:51], 0
	v_mov_b64_e32 v[52:53], 0
	v_mov_b64_e32 v[54:55], 0
	v_mov_b64_e32 v[56:57], 0
	v_mov_b64_e32 v[58:59], 0
	v_mov_b64_e32 v[60:61], 0
	v_mov_b64_e32 v[62:63], 0
	v_mov_b64_e32 v[64:65], 0
	v_mov_b64_e32 v[66:67], 0
	v_mov_b64_e32 v[68:69], 0
	v_mov_b64_e32 v[70:71], 0
	v_mov_b64_e32 v[72:73], 0
	v_mov_b64_e32 v[74:75], 0
	v_mov_b64_e32 v[76:77], 0
	v_mov_b64_e32 v[78:79], 0
	v_mov_b64_e32 v[80:81], 0
	v_mov_b64_e32 v[82:83], 0
	v_mov_b64_e32 v[84:85], 0
	v_mov_b64_e32 v[86:87], 0
	v_mov_b64_e32 v[88:89], 0
	v_mov_b64_e32 v[90:91], 0
	v_mov_b64_e32 v[92:93], 0
	v_mov_b64_e32 v[94:95], 0
	v_mov_b64_e32 v[96:97], 0
	v_mov_b64_e32 v[98:99], 0
	v_mov_b64_e32 v[100:101], 0
	v_mov_b64_e32 v[102:103], 0
	v_mov_b64_e32 v[104:105], 0
	v_mov_b64_e32 v[106:107], 0
	v_mov_b64_e32 v[108:109], 0
	v_mov_b64_e32 v[110:111], 0
	v_mov_b64_e32 v[112:113], 0
	v_mov_b64_e32 v[114:115], 0
	v_mov_b64_e32 v[116:117], 0
	v_mov_b64_e32 v[118:119], 0
	v_mov_b64_e32 v[120:121], 0
	v_mov_b64_e32 v[122:123], 0
	v_mov_b64_e32 v[124:125], 0
	v_mov_b64_e32 v[126:127], 0
	v_mov_b64_e32 v[128:129], 0
	v_mov_b64_e32 v[130:131], 0
	v_mov_b64_e32 v[132:133], 0
	v_mov_b64_e32 v[134:135], 0
	v_mov_b64_e32 v[136:137], 0
	v_mov_b64_e32 v[138:139], 0
	v_mov_b64_e32 v[140:141], 0
	v_mov_b64_e32 v[142:143], 0
	v_mov_b64_e32 v[144:145], 0
	v_mov_b64_e32 v[146:147], 0
	v_mov_b64_e32 v[148:149], 0
	v_mov_b64_e32 v[150:151], 0
	v_mov_b64_e32 v[152:153], 0
	v_mov_b64_e32 v[154:155], 0
	v_mov_b64_e32 v[156:157], 0
	v_mov_b64_e32 v[158:159], 0
	v_mov_b64_e32 v[160:161], 0

; template <class Epi, class Sched, bool ALIGN_EPI = true, bool F8 = false>
; __device__ __forceinline__ void gemm_phase(PG8_LAS unsigned char* lds, const Sched& S, const Epi& E) {
;     ...
; #pragma unroll
;         for (int a = 0; a < 2; ++a)
; #pragma unroll
;             for (int b = 0; b < 2; ++b)
; #pragma unroll
;                 for (int m = 0; m < 4; ++m)
; #pragma unroll
;                     for (int n = 0; n < 2; ++n) acc[a][b][m][n] = (f32x4){0.f, 0.f, 0.f, 0.f};
;         }
.LBB0_1137:
	s_add_u32 s23, s26, 0x10000
	s_addc_u32 s67, s27, 0
	s_add_u32 s24, s24, 0x8000
	v_mov_b64_e32 v[34:35], 0
	s_addc_u32 s25, s25, 0
	s_mov_b32 s68, -2
	v_mov_b64_e32 v[36:37], 0
	v_mov_b64_e32 v[38:39], 0
	v_mov_b64_e32 v[40:41], 0
	v_mov_b64_e32 v[50:51], 0
	v_mov_b64_e32 v[52:53], 0
	v_mov_b64_e32 v[54:55], 0
	v_mov_b64_e32 v[56:57], 0
	v_mov_b64_e32 v[66:67], 0
	v_mov_b64_e32 v[68:69], 0
	v_mov_b64_e32 v[70:71], 0
	v_mov_b64_e32 v[72:73], 0
	v_mov_b64_e32 v[82:83], 0
	v_mov_b64_e32 v[84:85], 0
	v_mov_b64_e32 v[86:87], 0
	v_mov_b64_e32 v[88:89], 0
	v_mov_b64_e32 v[42:43], 0
	v_mov_b64_e32 v[44:45], 0
	v_mov_b64_e32 v[46:47], 0
	v_mov_b64_e32 v[48:49], 0
	v_mov_b64_e32 v[58:59], 0
	v_mov_b64_e32 v[60:61], 0
	v_mov_b64_e32 v[62:63], 0
	v_mov_b64_e32 v[64:65], 0
	v_mov_b64_e32 v[74:75], 0
	v_mov_b64_e32 v[76:77], 0
	v_mov_b64_e32 v[78:79], 0
	v_mov_b64_e32 v[80:81], 0
	v_mov_b64_e32 v[90:91], 0
	v_mov_b64_e32 v[92:93], 0
	v_mov_b64_e32 v[94:95], 0
	v_mov_b64_e32 v[96:97], 0
	v_mov_b64_e32 v[98:99], 0
	v_mov_b64_e32 v[100:101], 0
	v_mov_b64_e32 v[102:103], 0
	v_mov_b64_e32 v[104:105], 0
	v_mov_b64_e32 v[114:115], 0
	v_mov_b64_e32 v[116:117], 0
	v_mov_b64_e32 v[118:119], 0
	v_mov_b64_e32 v[120:121], 0
	v_mov_b64_e32 v[130:131], 0
	v_mov_b64_e32 v[132:133], 0
	v_mov_b64_e32 v[134:135], 0
	v_mov_b64_e32 v[136:137], 0
	v_mov_b64_e32 v[146:147], 0
	v_mov_b64_e32 v[148:149], 0
	v_mov_b64_e32 v[150:151], 0
	v_mov_b64_e32 v[152:153], 0
	v_mov_b64_e32 v[106:107], 0
	v_mov_b64_e32 v[108:109], 0
	v_mov_b64_e32 v[110:111], 0
	v_mov_b64_e32 v[112:113], 0
	v_mov_b64_e32 v[122:123], 0
	v_mov_b64_e32 v[124:125], 0
	v_mov_b64_e32 v[126:127], 0
	v_mov_b64_e32 v[128:129], 0
	v_mov_b64_e32 v[138:139], 0
	v_mov_b64_e32 v[140:141], 0
	v_mov_b64_e32 v[142:143], 0
	v_mov_b64_e32 v[144:145], 0
	v_mov_b64_e32 v[154:155], 0
	v_mov_b64_e32 v[156:157], 0
	v_mov_b64_e32 v[158:159], 0
	v_mov_b64_e32 v[160:161], 0
	s_bitcmp1_b32 s3, 2
	s_cbranch_scc1 .Lh1e_33571
